# DA: next-tile LDS-DMA pieces interleaved into the QK MFMA stream (saddr form) instead of a burst after the barrier; Q fragment loads batched
# speedup vs baseline: 1.0198x; 1.0198x over previous
; #define LAS __attribute__((address_space(3)))
; __device__ __forceinline__ unsigned cvt_pk_bf16(float lo, float hi) { unsigned r; asm volatile("v_cvt_pk_bf16_f32 %0, %1, %2" : "=v"(r) : "v"(lo), "v"(hi)); return r; }
; __device__ __forceinline__ float bf_lo(unsigned w) { return __uint_as_float(w << 16); }
; __device__ __forceinline__ void attn_unit_da(const bf16_t* QKV, bf16_t* O, int b, int h, int qb, float slope2, int dmax, bool freeze_ok, const float* const* in, float lambda_init, LAS char* lds) {
;     const int tid = threadIdx.x, lane = tid & 63, r32 = lane & 31, hi = lane >> 5; const int wid = __builtin_amdgcn_readfirstlane(tid >> 6);
;     const int rg = wid & 3, c = wid >> 2;
;     const size_t rowb = (size_t)b * S; const int q0 = qb * 128, r0 = q0 + rg * 32;
;     const bf16_t* Kg0 = QKV + rowb * LDQ + D + h * 256; const bf16_t* Vg = QKV + rowb * LDQ + 2 * D + h * 256;
;     constexpr int STG = 4 * SHM_T;
;     LAS float* ws = (LAS float*)(lds + 2 * STG) + wid * 64;
;     bf16x8 qr[8];
;     { const bf16_t* Qw = QKV + (rowb + r0 + r32) * LDQ + h * 256 + c * 128 + hi * 8;
; #pragma unroll
;       for (int d0 = 0; d0 < 8; ++d0) { const u32x4 w = *(const u32x4*)(Qw + d0 * 16);
;           u32x4 o_; o_.x = cvt_pk_bf16(bf_lo(w.x) * QK_C, bf_hi(w.x) * QK_C); o_.y = cvt_pk_bf16(bf_lo(w.y) * QK_C, bf_hi(w.y) * QK_C); o_.z = cvt_pk_bf16(bf_lo(w.z) * QK_C, bf_hi(w.z) * QK_C); o_.w = cvt_pk_bf16(bf_lo(w.w) * QK_C, bf_hi(w.w) * QK_C);
;           qr[d0] = __builtin_bit_cast(bf16x8, o_); } }
; __device__ __forceinline__ void attn_phase_da(const Frame& F, const Args& a) {
;     ...
;         __syncthreads();
;         if (F.tid == 0) ubox[0] = __hip_atomic_fetch_add(qctr, 1u, __ATOMIC_RELAXED, __HIP_MEMORY_SCOPE_AGENT);
;         __syncthreads();
;         const unsigned u = ubox[0];
;         if (u >= 1024u) break;
;         const int h = 7 - (int)(u >> 7), rem = (int)(u & 127u), qb = 31 - (rem >> 2), b = rem & 3;
;         const float slope2 = exp2f(-(float)(h + 1)) * LOG2E;
;         const float dm = (150.f + 2.f * zb2) / slope2; const int dmax = dm < 1.0e6f ? (int)dm + 1 : 1000000;
;         const bool freeze_ok = (2.f * zb2 + 32.f * slope2) < 100.f;
;         att::attn_unit_da((const bf16_t*)(a.ws + WS_QKV), (bf16_t*)(a.ws + WS_O), b, h, qb, slope2, dmax, freeze_ok, a.in, lambda_init, (LAS char*)F.lds); }
.LBB0_1130:
	s_or_b64 exec, exec, s[0:1]
	s_waitcnt lgkmcnt(0)
	s_barrier
	ds_read_b32 v2, v237
	s_movk_i32 s0, 0x3ff
	s_waitcnt lgkmcnt(0)
	v_cmp_lt_u32_e32 vcc, s0, v2
	v_readfirstlane_b32 s2, v2
	s_mov_b64 s[0:1], -1
	s_cbranch_vccnz .LBB0_1125
	s_lshr_b32 s11, s2, 7
	s_not_b32 s0, s2
	s_bfe_u32 s4, s0, 0x50002
	s_sub_i32 s0, 8, s11
	v_cvt_f32_ubyte0_e32 v2, s0
	s_mov_b32 s0, 0x42fc0000
	v_cmp_lt_f32_e32 vcc, s0, v2
	s_and_b32 s5, s2, 3
	s_and_b64 s[0:1], vcc, exec
	v_cndmask_b32_e32 v4, 0, v238, vcc
	v_sub_f32_e32 v2, v4, v2
	v_exp_f32_e32 v2, v2
	s_cselect_b32 s0, 0xffffffc0, 0
	v_readfirstlane_b32 s2, v0
	s_bfe_u32 s68, s2, 0x20006
	v_ldexp_f32 v2, v2, s0
	v_mul_f32_e32 v212, 0x3fb8aa3b, v2
	v_mov_b32_e32 v4, 0xc2960000
	v_fmac_f32_e32 v4, 0.5, v1
	v_fmac_f32_e32 v4, 0x42000000, v212
	s_nop 0
	v_readfirstlane_b32 s98, v4
	v_div_scale_f32 v2, s[0:1], v212, v212, v1
	v_rcp_f32_e32 v4, v2
	s_mov_b32 s0, 0x49742400
	s_lshl_b32 s7, s4, 7
	s_lshl_b32 s9, s68, 5
	v_fma_f32 v5, -v2, v4, 1.0
	v_fmac_f32_e32 v4, v5, v4
	v_div_scale_f32 v5, vcc, v1, v212, v1
	v_mul_f32_e32 v6, v5, v4
	v_fma_f32 v7, -v2, v6, v5
	v_fmac_f32_e32 v6, v7, v4
	v_fma_f32 v2, -v2, v6, v5
	v_div_fmas_f32 v2, v2, v4, v6
	v_div_fixup_f32 v2, v2, v212, v1
	v_cmp_gt_f32_e32 vcc, s0, v2
	v_cvt_i32_f32_e32 v2, v2
	s_lshr_b32 s6, s2, 6
	s_lshr_b32 s3, s2, 8
	s_lshl_b32 s12, s5, 12
	s_or_b32 s69, s9, s7
	s_mul_i32 s8, s5, 0x3000000
	v_readlane_b32 s14, v255, 18
	v_readlane_b32 s15, v255, 19
	s_add_u32 s5, s14, s8
	v_add_u32_e32 v2, 1, v2
	s_addc_u32 s10, s15, 0
	s_or_b32 s52, s69, s12
	v_cndmask_b32_e32 v213, v239, v2, vcc
	v_or_b32_e32 v2, s52, v226
	s_lshl_b32 s0, s11, 8
	v_mul_u32_u24_e32 v2, 0x1800, v2
	s_sub_i32 s66, 0x700, s0
	v_lshlrev_b32_e32 v2, 1, v2
	s_lshl_b32 s0, s66, 1
	s_mov_b32 s1, s67
	v_lshl_add_u64 v[4:5], s[14:15], 0, v[2:3]
	v_lshl_add_u64 v[4:5], v[4:5], 0, s[0:1]
	s_and_b32 s12, s2, 0xffffff00
	s_mov_b32 s13, s67
	v_lshl_add_u64 v[4:5], v[4:5], 0, s[12:13]
	v_mov_b32_e32 v211, v3
	v_lshl_add_u64 v[4:5], v[4:5], 0, v[210:211]
	global_load_dwordx4 v[178:181], v[4:5], off
	global_load_dwordx4 v[182:185], v[4:5], off offset:32
	global_load_dwordx4 v[186:189], v[4:5], off offset:64
	global_load_dwordx4 v[190:193], v[4:5], off offset:96
	global_load_dwordx4 v[194:197], v[4:5], off offset:128
	global_load_dwordx4 v[198:201], v[4:5], off offset:160
	global_load_dwordx4 v[202:205], v[4:5], off offset:192
	global_load_dwordx4 v[206:209], v[4:5], off offset:224
	s_and_b32 s11, s2, 0x3fffffc0
	s_lshl_b32 s1, s11, 2
	s_add_i32 s70, s1, 0
	s_add_i32 s70, s70, 0x20000
	s_add_u32 s0, s5, s0
	s_addc_u32 s1, s10, 0
	s_lshl_b32 s71, s6, 2
	s_mul_i32 s11, s4, 0x180000
	s_lshl_b32 s10, s4, 1
	s_lshl_b32 s90, s6, 1
	s_add_i32 s4, s11, 0xc0000
	s_add_u32 s0, s0, s4
	s_addc_u32 s1, s1, 0
	s_add_u32 s4, s0, 0x1000
	s_addc_u32 s5, s1, 0
	s_lshl_b32 s12, s6, 10
	s_add_i32 s91, s12, 0
	s_add_i32 s14, s91, 0x4000
	s_add_u32 s0, s0, 0x2000
	s_mov_b32 m0, s91
	s_addc_u32 s1, s1, 0
	s_add_i32 s13, s91, 0x8000
	s_add_i32 s12, s91, 0xc000
	v_mov_b32_e32 v11, v3
	v_mov_b32_e32 v16, v3
	v_mov_b32_e32 v17, v3
	v_mov_b32_e32 v14, v3
	v_mov_b32_e32 v15, v3
	v_mov_b32_e32 v214, 0
	s_waitcnt vmcnt(7)
	v_lshlrev_b32_e32 v2, 16, v178
	v_and_b32_e32 v6, 0xffff0000, v178
	v_mul_f32_e32 v6, 0x3e0293ee, v6
	v_mul_f32_e32 v2, 0x3e0293ee, v2
	v_cvt_pk_bf16_f32 v178, v2, v6
	v_lshlrev_b32_e32 v2, 16, v179
	v_and_b32_e32 v6, 0xffff0000, v179
	v_mul_f32_e32 v6, 0x3e0293ee, v6
	v_mul_f32_e32 v2, 0x3e0293ee, v2
	v_cvt_pk_bf16_f32 v179, v2, v6
	v_lshlrev_b32_e32 v2, 16, v180
	v_and_b32_e32 v6, 0xffff0000, v180
	v_mul_f32_e32 v6, 0x3e0293ee, v6
	v_mul_f32_e32 v2, 0x3e0293ee, v2
	v_cvt_pk_bf16_f32 v180, v2, v6
	v_lshlrev_b32_e32 v2, 16, v181
	v_and_b32_e32 v6, 0xffff0000, v181
	v_mul_f32_e32 v6, 0x3e0293ee, v6
	v_mul_f32_e32 v2, 0x3e0293ee, v2
	v_cvt_pk_bf16_f32 v181, v2, v6
	s_waitcnt vmcnt(6)
	v_lshlrev_b32_e32 v2, 16, v182
	v_and_b32_e32 v6, 0xffff0000, v182
	v_mul_f32_e32 v6, 0x3e0293ee, v6
	v_mul_f32_e32 v2, 0x3e0293ee, v2
	v_cvt_pk_bf16_f32 v182, v2, v6
	v_lshlrev_b32_e32 v2, 16, v183
	v_and_b32_e32 v6, 0xffff0000, v183
	v_mul_f32_e32 v6, 0x3e0293ee, v6
	v_mul_f32_e32 v2, 0x3e0293ee, v2
	v_cvt_pk_bf16_f32 v183, v2, v6
	v_lshlrev_b32_e32 v2, 16, v184
	v_and_b32_e32 v6, 0xffff0000, v184
	v_mul_f32_e32 v6, 0x3e0293ee, v6
	v_mul_f32_e32 v2, 0x3e0293ee, v2
	v_cvt_pk_bf16_f32 v184, v2, v6
	v_lshlrev_b32_e32 v2, 16, v185
	v_and_b32_e32 v6, 0xffff0000, v185
	v_mul_f32_e32 v6, 0x3e0293ee, v6
	v_mul_f32_e32 v2, 0x3e0293ee, v2
	v_cvt_pk_bf16_f32 v185, v2, v6
	s_waitcnt vmcnt(5)
	v_lshlrev_b32_e32 v2, 16, v186
	v_and_b32_e32 v6, 0xffff0000, v186
	v_mul_f32_e32 v6, 0x3e0293ee, v6
	v_mul_f32_e32 v2, 0x3e0293ee, v2
	v_cvt_pk_bf16_f32 v186, v2, v6
	v_lshlrev_b32_e32 v2, 16, v187
	v_and_b32_e32 v6, 0xffff0000, v187
	v_mul_f32_e32 v6, 0x3e0293ee, v6
	v_mul_f32_e32 v2, 0x3e0293ee, v2
	v_cvt_pk_bf16_f32 v187, v2, v6
	v_lshlrev_b32_e32 v2, 16, v188
	v_and_b32_e32 v6, 0xffff0000, v188
	v_mul_f32_e32 v6, 0x3e0293ee, v6
	v_mul_f32_e32 v2, 0x3e0293ee, v2
	v_cvt_pk_bf16_f32 v188, v2, v6
	v_lshlrev_b32_e32 v2, 16, v189
	v_and_b32_e32 v6, 0xffff0000, v189
	v_mul_f32_e32 v6, 0x3e0293ee, v6
	v_mul_f32_e32 v2, 0x3e0293ee, v2
	v_cvt_pk_bf16_f32 v189, v2, v6
	s_waitcnt vmcnt(4)
	v_lshlrev_b32_e32 v2, 16, v190
	v_and_b32_e32 v6, 0xffff0000, v190
	v_mul_f32_e32 v6, 0x3e0293ee, v6
	v_mul_f32_e32 v2, 0x3e0293ee, v2
	v_cvt_pk_bf16_f32 v190, v2, v6
	v_lshlrev_b32_e32 v2, 16, v191
	v_and_b32_e32 v6, 0xffff0000, v191
	v_mul_f32_e32 v6, 0x3e0293ee, v6
	v_mul_f32_e32 v2, 0x3e0293ee, v2
	v_cvt_pk_bf16_f32 v191, v2, v6
	v_lshlrev_b32_e32 v2, 16, v192
	v_and_b32_e32 v6, 0xffff0000, v192
	v_mul_f32_e32 v6, 0x3e0293ee, v6
	v_mul_f32_e32 v2, 0x3e0293ee, v2
	v_cvt_pk_bf16_f32 v192, v2, v6
	v_lshlrev_b32_e32 v2, 16, v193
	v_and_b32_e32 v6, 0xffff0000, v193
	v_mul_f32_e32 v6, 0x3e0293ee, v6
	v_mul_f32_e32 v2, 0x3e0293ee, v2
	v_cvt_pk_bf16_f32 v193, v2, v6
	s_waitcnt vmcnt(3)
; __device__ __forceinline__ unsigned cvt_pk_bf16(float lo, float hi) { unsigned r; asm volatile("v_cvt_pk_bf16_f32 %0, %1, %2" : "=v"(r) : "v"(lo), "v"(hi)); return r; }
; __device__ __forceinline__ float bf_lo(unsigned w) { return __uint_as_float(w << 16); }
; __device__ __forceinline__ float bf_hi(unsigned w) { return __uint_as_float(w & 0xffff0000u); }
; __device__ __forceinline__ void attn_unit_da(const bf16_t* QKV, bf16_t* O, int b, int h, int qb, float slope2, int dmax, bool freeze_ok, const float* const* in, float lambda_init, LAS char* lds) {
;     ...
;       for (int d0 = 0; d0 < 8; ++d0) { const u32x4 w = *(const u32x4*)(Qw + d0 * 16);
;           u32x4 o_; o_.x = cvt_pk_bf16(bf_lo(w.x) * QK_C, bf_hi(w.x) * QK_C); o_.y = cvt_pk_bf16(bf_lo(w.y) * QK_C, bf_hi(w.y) * QK_C); o_.z = cvt_pk_bf16(bf_lo(w.z) * QK_C, bf_hi(w.z) * QK_C); o_.w = cvt_pk_bf16(bf_lo(w.w) * QK_C, bf_hi(w.w) * QK_C);
;           qr[d0] = __builtin_bit_cast(bf16x8, o_); } }
;     ...
;     const int NT = 2 * (qb + 1);
;     int kt_lo = 0; { const int lim = q0 - 63 - dmax; kt_lo = lim > 0 ? (lim + 63) / 64 : 0; }
;     const int NIT = NT - kt_lo;
;     DMA_DA((NT - 1) * KVBLK, 0);
	v_lshlrev_b32_e32 v2, 16, v194
	v_and_b32_e32 v6, 0xffff0000, v194
	v_mul_f32_e32 v6, 0x3e0293ee, v6
	v_mul_f32_e32 v2, 0x3e0293ee, v2
	v_cvt_pk_bf16_f32 v194, v2, v6
	v_lshlrev_b32_e32 v2, 16, v195
	v_and_b32_e32 v6, 0xffff0000, v195
	v_mul_f32_e32 v6, 0x3e0293ee, v6
	v_mul_f32_e32 v2, 0x3e0293ee, v2
	v_cvt_pk_bf16_f32 v195, v2, v6
	v_lshlrev_b32_e32 v2, 16, v196
	v_and_b32_e32 v6, 0xffff0000, v196
	v_mul_f32_e32 v6, 0x3e0293ee, v6
	v_mul_f32_e32 v2, 0x3e0293ee, v2
	v_cvt_pk_bf16_f32 v196, v2, v6
	v_lshlrev_b32_e32 v2, 16, v197
	v_and_b32_e32 v6, 0xffff0000, v197
	v_mul_f32_e32 v6, 0x3e0293ee, v6
	v_mul_f32_e32 v2, 0x3e0293ee, v2
	v_cvt_pk_bf16_f32 v197, v2, v6
	s_waitcnt vmcnt(2)
	v_lshlrev_b32_e32 v2, 16, v198
	v_and_b32_e32 v6, 0xffff0000, v198
	v_mul_f32_e32 v6, 0x3e0293ee, v6
	v_mul_f32_e32 v2, 0x3e0293ee, v2
	v_cvt_pk_bf16_f32 v198, v2, v6
	v_lshlrev_b32_e32 v2, 16, v199
	v_and_b32_e32 v6, 0xffff0000, v199
	v_mul_f32_e32 v6, 0x3e0293ee, v6
	v_mul_f32_e32 v2, 0x3e0293ee, v2
	v_cvt_pk_bf16_f32 v199, v2, v6
	v_lshlrev_b32_e32 v2, 16, v200
	v_and_b32_e32 v6, 0xffff0000, v200
	v_mul_f32_e32 v6, 0x3e0293ee, v6
	v_mul_f32_e32 v2, 0x3e0293ee, v2
	v_cvt_pk_bf16_f32 v200, v2, v6
	v_lshlrev_b32_e32 v2, 16, v201
	v_and_b32_e32 v6, 0xffff0000, v201
	v_mul_f32_e32 v6, 0x3e0293ee, v6
	v_mul_f32_e32 v2, 0x3e0293ee, v2
	v_cvt_pk_bf16_f32 v201, v2, v6
	s_waitcnt vmcnt(1)
	v_lshlrev_b32_e32 v2, 16, v202
	v_and_b32_e32 v6, 0xffff0000, v202
	v_mul_f32_e32 v6, 0x3e0293ee, v6
	v_mul_f32_e32 v2, 0x3e0293ee, v2
	v_cvt_pk_bf16_f32 v202, v2, v6
	v_lshlrev_b32_e32 v2, 16, v203
	v_and_b32_e32 v6, 0xffff0000, v203
	v_mul_f32_e32 v6, 0x3e0293ee, v6
	v_mul_f32_e32 v2, 0x3e0293ee, v2
	v_cvt_pk_bf16_f32 v203, v2, v6
	v_lshlrev_b32_e32 v2, 16, v204
	v_and_b32_e32 v6, 0xffff0000, v204
	v_mul_f32_e32 v6, 0x3e0293ee, v6
	v_mul_f32_e32 v2, 0x3e0293ee, v2
	v_cvt_pk_bf16_f32 v204, v2, v6
	v_lshlrev_b32_e32 v2, 16, v205
	v_and_b32_e32 v6, 0xffff0000, v205
	v_mul_f32_e32 v6, 0x3e0293ee, v6
	v_mul_f32_e32 v2, 0x3e0293ee, v2
	v_cvt_pk_bf16_f32 v205, v2, v6
	s_waitcnt vmcnt(0)
	v_lshlrev_b32_e32 v2, 16, v206
	v_and_b32_e32 v6, 0xffff0000, v206
	v_mul_f32_e32 v6, 0x3e0293ee, v6
	v_mul_f32_e32 v2, 0x3e0293ee, v2
	v_cvt_pk_bf16_f32 v206, v2, v6
	v_lshlrev_b32_e32 v2, 16, v207
	v_and_b32_e32 v6, 0xffff0000, v207
	v_mul_f32_e32 v6, 0x3e0293ee, v6
	v_mul_f32_e32 v2, 0x3e0293ee, v2
	v_cvt_pk_bf16_f32 v207, v2, v6
	v_lshlrev_b32_e32 v2, 16, v208
	v_and_b32_e32 v6, 0xffff0000, v208
	v_mul_f32_e32 v6, 0x3e0293ee, v6
	v_mul_f32_e32 v2, 0x3e0293ee, v2
	v_cvt_pk_bf16_f32 v208, v2, v6
	v_lshlrev_b32_e32 v2, 16, v209
	v_and_b32_e32 v6, 0xffff0000, v209
	v_mul_f32_e32 v6, 0x3e0293ee, v6
	v_mul_f32_e32 v2, 0x3e0293ee, v2
	v_cvt_pk_bf16_f32 v209, v2, v6
	v_sub_u32_e32 v2, s7, v213
	v_subrev_u32_e32 v4, 63, v2
	v_cmp_lt_i32_e32 vcc, 0, v4
	v_lshrrev_b32_e32 v2, 6, v2
	s_nop 0
	v_cndmask_b32_e32 v6, 0, v2, vcc
	v_mov_b32_e32 v2, v230
	s_nop 0
	v_ashrrev_i32_e32 v4, 4, v2
	v_add_u32_e32 v4, s71, v4
	v_lshlrev_b32_e32 v5, 4, v2
	v_and_b32_e32 v5, 0xf0, v5
	v_lshlrev_b32_e32 v7, 4, v4
	v_bitop3_b32 v5, v7, v5, s45 bitop3:0x6c
	v_ashrrev_i32_e32 v7, 5, v2
	v_add_u32_e32 v7, s90, v7
	v_bfe_u32 v8, v2, 2, 2
	v_lshrrev_b32_e32 v9, 1, v2
	v_lshlrev_b32_e32 v2, 3, v2
	v_lshrrev_b32_e32 v5, 1, v5
	v_and_or_b32 v8, v9, 8, v8
	v_and_b32_e32 v9, 24, v2
	v_mul_lo_u32 v2, v4, s79
	v_lshlrev_b32_e32 v4, 1, v7
	v_or_b32_e32 v2, v5, v2
	v_lshlrev_b32_e32 v250, 1, v2
	v_and_b32_e32 v4, 0x1ffff0, v4
	v_and_b32_e32 v5, 4, v7
	v_or3_b32 v4, v8, v5, v4
	v_lshlrev_b32_e32 v5, 5, v7
	v_and_b32_e32 v5, 0x60, v5
	v_mul_u32_u24_e32 v4, 0x1800, v4
	v_lshl_add_u64 v[12:13], v[2:3], 1, s[4:5]
	v_or3_b32 v8, v5, v9, v4
	v_lshlrev_b32_e32 v251, 1, v8
	global_load_lds_dwordx4 v[12:13], off
	v_lshl_add_u64 v[12:13], v[12:13], 0, s[38:39]
	s_mov_b32 m0, s14
	v_mov_b32_e32 v9, v3
	v_add_u32_e32 v4, 0x30000, v8
	global_load_lds_dwordx4 v[12:13], off
	v_lshl_add_u64 v[8:9], v[8:9], 1, s[0:1]
	s_mov_b32 m0, s13
	v_add_u32_e32 v10, 0x30000, v2
	global_load_lds_dwordx4 v[8:9], off
	v_lshl_add_u64 v[8:9], v[8:9], 0, s[38:39]
	s_mov_b32 m0, s12
	v_mov_b32_e32 v5, v3
	global_load_lds_dwordx4 v[8:9], off
	v_lshl_add_u64 v[8:9], v[10:11], 1, s[4:5]
	s_add_i32 m0, s91, 0x2000
	v_lshl_add_u64 v[4:5], v[4:5], 1, s[0:1]
	global_load_lds_dwordx4 v[8:9], off
	v_lshl_add_u64 v[8:9], v[8:9], 0, s[38:39]
	s_add_i32 m0, s91, 0x6000
	v_sub_u32_e32 v2, s10, v6
	global_load_lds_dwordx4 v[8:9], off
	s_add_i32 m0, s91, 0xa000
	v_add_u32_e32 v211, 2, v2
	global_load_lds_dwordx4 v[4:5], off
	v_lshl_add_u64 v[4:5], v[4:5], 0, s[38:39]
	s_add_i32 m0, s91, 0xe000
	v_mov_b32_e32 v2, v3
	global_load_lds_dwordx4 v[4:5], off
	v_mov_b32_e32 v4, v3
	v_mov_b32_e32 v5, v3
	v_mov_b32_e32 v6, v3
	v_mov_b32_e32 v7, v3
	v_mov_b32_e32 v8, v3
	v_mov_b32_e32 v9, v3
	v_mov_b32_e32 v10, v3
	v_mov_b32_e32 v12, v3
	v_mov_b32_e32 v13, v3
	v_mov_b64_e32 v[32:33], v[16:17]
	v_mov_b64_e32 v[48:49], v[16:17]
	v_mov_b64_e32 v[64:65], v[16:17]
	v_mov_b64_e32 v[80:81], v[16:17]
	v_mov_b64_e32 v[96:97], v[16:17]
	v_mov_b64_e32 v[112:113], v[16:17]
; __device__ __forceinline__ void attn_unit_da(const bf16_t* QKV, bf16_t* O, int b, int h, int qb, float slope2, int dmax, bool freeze_ok, const float* const* in, float lambda_init, LAS char* lds) {
;     ...
;     f32x16 o[8];
; #pragma unroll
;     for (int d = 0; d < 8; ++d) o[d] = f32x16{};
;     ...
;     const int NT = 2 * (qb + 1);
;     int kt_lo = 0; { const int lim = q0 - 63 - dmax; kt_lo = lim > 0 ? (lim + 63) / 64 : 0; }
;     const int NIT = NT - kt_lo;
;     DMA_DA((NT - 1) * KVBLK, 0);
;     float m_run = -1e30f, l_run = 0.f;
;     for (int it = 0; it < NIT; ++it) {
	v_mov_b64_e32 v[128:129], v[16:17]
	v_mov_b64_e32 v[144:145], v[16:17]
	v_cmp_lt_i32_e32 vcc, 0, v211
	v_mov_b64_e32 v[30:31], v[14:15]
	v_mov_b64_e32 v[28:29], v[12:13]
	v_mov_b64_e32 v[26:27], v[10:11]
	v_mov_b64_e32 v[24:25], v[8:9]
	v_mov_b64_e32 v[22:23], v[6:7]
	v_mov_b64_e32 v[20:21], v[4:5]
	v_mov_b64_e32 v[18:19], v[2:3]
	v_mov_b64_e32 v[46:47], v[14:15]
	v_mov_b64_e32 v[44:45], v[12:13]
	v_mov_b64_e32 v[42:43], v[10:11]
	v_mov_b64_e32 v[40:41], v[8:9]
	v_mov_b64_e32 v[38:39], v[6:7]
	v_mov_b64_e32 v[36:37], v[4:5]
	v_mov_b64_e32 v[34:35], v[2:3]
	v_mov_b64_e32 v[62:63], v[14:15]
	v_mov_b64_e32 v[60:61], v[12:13]
	v_mov_b64_e32 v[58:59], v[10:11]
	v_mov_b64_e32 v[56:57], v[8:9]
	v_mov_b64_e32 v[54:55], v[6:7]
	v_mov_b64_e32 v[52:53], v[4:5]
	v_mov_b64_e32 v[50:51], v[2:3]
	v_mov_b64_e32 v[78:79], v[14:15]
	v_mov_b64_e32 v[76:77], v[12:13]
	v_mov_b64_e32 v[74:75], v[10:11]
	v_mov_b64_e32 v[72:73], v[8:9]
	v_mov_b64_e32 v[70:71], v[6:7]
	v_mov_b64_e32 v[68:69], v[4:5]
	v_mov_b64_e32 v[66:67], v[2:3]
	v_mov_b64_e32 v[94:95], v[14:15]
	v_mov_b64_e32 v[92:93], v[12:13]
	v_mov_b64_e32 v[90:91], v[10:11]
	v_mov_b64_e32 v[88:89], v[8:9]
	v_mov_b64_e32 v[86:87], v[6:7]
	v_mov_b64_e32 v[84:85], v[4:5]
	v_mov_b64_e32 v[82:83], v[2:3]
	v_mov_b64_e32 v[110:111], v[14:15]
	v_mov_b64_e32 v[108:109], v[12:13]
	v_mov_b64_e32 v[106:107], v[10:11]
	v_mov_b64_e32 v[104:105], v[8:9]
	v_mov_b64_e32 v[102:103], v[6:7]
	v_mov_b64_e32 v[100:101], v[4:5]
	v_mov_b64_e32 v[98:99], v[2:3]
	v_mov_b64_e32 v[126:127], v[14:15]
	v_mov_b64_e32 v[124:125], v[12:13]
	v_mov_b64_e32 v[122:123], v[10:11]
	v_mov_b64_e32 v[120:121], v[8:9]
	v_mov_b64_e32 v[118:119], v[6:7]
	v_mov_b64_e32 v[116:117], v[4:5]
	v_mov_b64_e32 v[114:115], v[2:3]
	v_mov_b64_e32 v[142:143], v[14:15]
	v_mov_b64_e32 v[140:141], v[12:13]
	v_mov_b64_e32 v[138:139], v[10:11]
	v_mov_b64_e32 v[136:137], v[8:9]
	v_mov_b64_e32 v[134:135], v[6:7]
	v_mov_b64_e32 v[132:133], v[4:5]
	v_mov_b64_e32 v[130:131], v[2:3]
	s_and_saveexec_b64 s[4:5], vcc
	s_cbranch_execz .LBB0_1145
	s_lshl_b32 s0, s3, 14
	s_mov_b64 s[82:83], s[96:97]
	s_add_i32 s96, s0, 0
	s_sub_i32 s97, 64, s9
	s_add_i32 s80, s7, 0x7f
	s_add_u32 s0, s8, s11
	s_mul_i32 s81, s6, 0x6000
	s_addc_u32 s1, 0, 0
	s_lshl_b32 s6, s66, 1
	s_add_u32 s0, s0, s6
	s_addc_u32 s1, s1, 0
	v_readlane_b32 s6, v255, 48
	v_mov_b32_e32 v16, v3
	v_mov_b32_e32 v17, v3
	s_add_u32 s72, s6, s0
	v_readlane_b32 s0, v255, 49
	v_mov_b32_e32 v2, v3
	v_mov_b32_e32 v4, v3
	v_mov_b32_e32 v5, v3
	v_mov_b32_e32 v6, v3
	v_mov_b32_e32 v7, v3
	v_mov_b32_e32 v8, v3
	v_mov_b32_e32 v9, v3
	v_mov_b32_e32 v10, v3
	v_mov_b32_e32 v11, v3
	v_mov_b32_e32 v12, v3
	v_mov_b32_e32 v13, v3
	v_mov_b32_e32 v14, v3
	v_mov_b32_e32 v15, v3
	v_mov_b64_e32 v[144:145], v[16:17]
	v_mov_b64_e32 v[128:129], v[16:17]
	v_mov_b64_e32 v[112:113], v[16:17]
	v_mov_b64_e32 v[96:97], v[16:17]
	v_mov_b64_e32 v[80:81], v[16:17]
	v_mov_b64_e32 v[64:65], v[16:17]
	v_mov_b64_e32 v[48:49], v[16:17]
	v_mov_b64_e32 v[32:33], v[16:17]
	s_mov_b32 s78, s52
	s_mov_b32 s33, s93
	s_mov_b32 s86, 1
	s_addc_u32 s73, s0, s1
	s_add_i32 s87, s81, 0x30000
	v_mov_b32_e32 v214, 0
	v_mov_b32_e32 v215, 0xf149f2ca
	s_mov_b64 s[92:93], 0
	v_mov_b64_e32 v[142:143], v[14:15]
	v_mov_b64_e32 v[140:141], v[12:13]
	v_mov_b64_e32 v[138:139], v[10:11]
	v_mov_b64_e32 v[136:137], v[8:9]
	v_mov_b64_e32 v[134:135], v[6:7]
	v_mov_b64_e32 v[132:133], v[4:5]
	v_mov_b64_e32 v[130:131], v[2:3]
	v_mov_b64_e32 v[126:127], v[14:15]
	v_mov_b64_e32 v[124:125], v[12:13]
	v_mov_b64_e32 v[122:123], v[10:11]
	v_mov_b64_e32 v[120:121], v[8:9]
	v_mov_b64_e32 v[118:119], v[6:7]
	v_mov_b64_e32 v[116:117], v[4:5]
	v_mov_b64_e32 v[114:115], v[2:3]
	v_mov_b64_e32 v[110:111], v[14:15]
	v_mov_b64_e32 v[108:109], v[12:13]
	v_mov_b64_e32 v[106:107], v[10:11]
	v_mov_b64_e32 v[104:105], v[8:9]
	v_mov_b64_e32 v[102:103], v[6:7]
	v_mov_b64_e32 v[100:101], v[4:5]
	v_mov_b64_e32 v[98:99], v[2:3]
	v_mov_b64_e32 v[94:95], v[14:15]
	v_mov_b64_e32 v[92:93], v[12:13]
	v_mov_b64_e32 v[90:91], v[10:11]
	v_mov_b64_e32 v[88:89], v[8:9]
	v_mov_b64_e32 v[86:87], v[6:7]
	v_mov_b64_e32 v[84:85], v[4:5]
	v_mov_b64_e32 v[82:83], v[2:3]
	v_mov_b64_e32 v[78:79], v[14:15]
	v_mov_b64_e32 v[76:77], v[12:13]
	v_mov_b64_e32 v[74:75], v[10:11]
	v_mov_b64_e32 v[72:73], v[8:9]
	v_mov_b64_e32 v[70:71], v[6:7]
	v_mov_b64_e32 v[68:69], v[4:5]
	v_mov_b64_e32 v[66:67], v[2:3]
	v_mov_b64_e32 v[62:63], v[14:15]
	v_mov_b64_e32 v[60:61], v[12:13]
	v_mov_b64_e32 v[58:59], v[10:11]
	v_mov_b64_e32 v[56:57], v[8:9]
	v_mov_b64_e32 v[54:55], v[6:7]
	v_mov_b64_e32 v[52:53], v[4:5]
	v_mov_b64_e32 v[50:51], v[2:3]
	v_mov_b64_e32 v[46:47], v[14:15]
	v_mov_b64_e32 v[44:45], v[12:13]
	v_mov_b64_e32 v[42:43], v[10:11]
	v_mov_b64_e32 v[40:41], v[8:9]
	v_mov_b64_e32 v[38:39], v[6:7]
	v_mov_b64_e32 v[36:37], v[4:5]
	v_mov_b64_e32 v[34:35], v[2:3]
	v_mov_b64_e32 v[30:31], v[14:15]
	v_mov_b64_e32 v[28:29], v[12:13]
	v_mov_b64_e32 v[26:27], v[10:11]
	v_mov_b64_e32 v[24:25], v[8:9]
	v_mov_b64_e32 v[22:23], v[6:7]
	v_mov_b64_e32 v[20:21], v[4:5]
	v_mov_b64_e32 v[18:19], v[2:3]
	s_branch .LBB0_1136

; #define LAS __attribute__((address_space(3)))
; #define QKRD(S, KB, OFF) do { S##0 = *(const LAS bf16x8*)((KB) + (OFF)); S##1 = *(const LAS bf16x8*)((KB) + (OFF) + 8192); } while (0)
; __device__ __forceinline__ void attn_unit_da(const bf16_t* QKV, bf16_t* O, int b, int h, int qb, float slope2, int dmax, bool freeze_ok, const float* const* in, float lambda_init, LAS char* lds) {
;     ...
;     for (int it = 0; it < NIT; ++it) {
;         const int k0 = (NT - 1 - it) * KVBLK, bf = it & 1;
;         asm volatile("s_waitcnt vmcnt(0)" ::: "memory");
;         __syncthreads();
;         if (it + 1 < NIT) DMA_DA((NT - 2 - it) * KVBLK, bf ^ 1);
;         const bool active = (k0 <= r0) && (k0 + 63 + dmax >= r0);
;         if (active) {
;             int lt_ = lane; asm volatile("" : "+v"(lt_)); const int hi_t = lt_ >> 5, r32_t = lt_ & 31;
;             const float fb = slope2 * (float)(k0 - r0 + 4 * hi_t);
;             const bool need_mask = (k0 + 63 > r0);
;             const float cb = fb;
;             f32x16 p0, p1; float sl_ = slope2; asm volatile("" : "+v"(sl_));
; #pragma unroll
;             for (int r = 0; r < 16; ++r) { p0[r] = fmaf(sl_, (float)((r & 3) + 8 * (r >> 2)), cb); p1[r] = fmaf(sl_, (float)(32 + (r & 3) + 8 * (r >> 2)), cb); }
;             {
;               const LAS char* Ks = lds + bf * STG + c * SHM_T; int ln_ = lane; asm volatile("" : "+v"(ln_)); const int r32_ = ln_ & 31, hi_ = ln_ >> 5;
;               const LAS char* kb0 = Ks + (r32_ * 256 + (((0 * 2 + hi_) ^ (r32_ & 7)) << 4)); const LAS char* kb1 = Ks + (r32_ * 256 + (((1 * 2 + hi_) ^ (r32_ & 7)) << 4));
;               const LAS char* kb2 = Ks + (r32_ * 256 + (((2 * 2 + hi_) ^ (r32_ & 7)) << 4)); const LAS char* kb3 = Ks + (r32_ * 256 + (((3 * 2 + hi_) ^ (r32_ & 7)) << 4));
;               bf16x8 xa0, xa1, xb0, xb1;
;     ...
;               QKRD(xa, kb0, 0);
;               QKRD(xb, kb0, 128); QKMM(xa, 0, 2);
;               QKRD(xa, kb1, 0);   QKMM(xb, 4, 2);
;               QKRD(xb, kb1, 128); QKMM(xa, 1, 2);
;               QKRD(xa, kb2, 0);   QKMM(xb, 5, 2);
;               QKRD(xb, kb2, 128); QKMM(xa, 2, 2);
;               QKRD(xa, kb3, 0);   QKMM(xb, 6, 2);
;               QKRD(xb, kb3, 128); QKMM(xa, 3, 2);
;                                   QKMM(xb, 7, 0);
.LBB0_1136:
	s_waitcnt vmcnt(0)
	s_add_i32 s0, s86, -1
	s_and_b32 s8, s0, 1
	v_cmp_ge_i32_e64 s[0:1], s86, v211
	s_waitcnt vmcnt(0) lgkmcnt(0)
	s_barrier
	s_sub_i32 s6, s80, 63
	s_cmp_le_i32 s6, s69
	v_add_u32_e32 v2, s80, v213
	s_cselect_b64 s[6:7], -1, 0
	v_cmp_le_i32_e32 vcc, s69, v2
	s_and_b64 s[6:7], s[6:7], vcc
	s_and_saveexec_b64 s[76:77], s[6:7]
	s_cbranch_execz .Lda_inactive
	s_lshl_b32 s99, s8, 16
	s_xor_b32 s99, s99, 0x10000
	s_add_i32 s99, s91, s99
	v_mov_b32_e32 v5, v230
	s_lshl_b32 s94, s8, 16
	v_ashrrev_i32_e32 v2, 3, v5
	v_and_b32_e32 v4, -4, v2
	v_add_u32_e32 v2, s97, v4
	v_cvt_f32_i32_e32 v7, v2
	v_mov_b32_e32 v2, v212
	s_add_i32 s6, s96, s94
	v_mul_f32_e32 v6, v212, v7
	v_subrev_f32_e32 v6, s98, v6
	v_fma_f32 v146, 0, v2, v6
	v_pk_fma_f32 v[148:149], v[2:3], s[16:17], v[6:7] op_sel_hi:[0,1,0]
	v_pk_fma_f32 v[150:151], v[2:3], s[18:19], v[6:7] op_sel_hi:[0,1,0]
	v_pk_fma_f32 v[152:153], v[2:3], s[20:21], v[6:7] op_sel_hi:[0,1,0]
	v_pk_fma_f32 v[154:155], v[2:3], s[22:23], v[6:7] op_sel_hi:[0,1,0]
	v_pk_fma_f32 v[156:157], v[2:3], s[24:25], v[6:7] op_sel_hi:[0,1,0]
	v_pk_fma_f32 v[158:159], v[2:3], s[26:27], v[6:7] op_sel_hi:[0,1,0]
	v_pk_fma_f32 v[160:161], v[2:3], s[28:29], v[6:7] op_sel_hi:[0,1,0]
	v_pk_fma_f32 v[176:177], v[2:3], s[30:31], v[6:7] op_sel_hi:[0,1,0]
	v_pk_fma_f32 v[174:175], v[2:3], s[34:35], v[6:7] op_sel_hi:[0,1,0]
	v_pk_fma_f32 v[172:173], v[2:3], s[36:37], v[6:7] op_sel_hi:[0,1,0]
	v_pk_fma_f32 v[170:171], v[2:3], s[40:41], v[6:7] op_sel_hi:[0,1,0]
	v_pk_fma_f32 v[168:169], v[2:3], s[42:43], v[6:7] op_sel_hi:[0,1,0]
	v_pk_fma_f32 v[166:167], v[2:3], s[46:47], v[6:7] op_sel_hi:[0,1,0]
	v_pk_fma_f32 v[164:165], v[2:3], s[48:49], v[6:7] op_sel_hi:[0,1,0]
	v_pk_fma_f32 v[162:163], v[2:3], s[50:51], v[6:7] op_sel_hi:[0,1,0]
	v_mov_b32_e32 v2, v230
	v_add_f32_e32 v147, v212, v6
	v_lshlrev_b32_e32 v8, 8, v2
	v_ashrrev_i32_e32 v7, 5, v2
	v_and_b32_e32 v8, 0x1f00, v8
	v_bitop3_b32 v9, v7, v2, 7 bitop3:0x78
	v_add_u32_e32 v8, s6, v8
	v_lshl_add_u32 v16, v9, 4, v8
	v_add_u32_e32 v9, 2, v7
	v_bitop3_b32 v9, v9, v2, 7 bitop3:0x78
	v_lshl_add_u32 v17, v9, 4, v8
	v_add_u32_e32 v9, 4, v7
	v_add_u32_e32 v7, 6, v7
	v_bitop3_b32 v9, v9, v2, 7 bitop3:0x78
	v_bitop3_b32 v2, v7, v2, 7 bitop3:0x78
	v_lshl_add_u32 v224, v9, 4, v8
	v_lshl_add_u32 v2, v2, 4, v8
	ds_read_b128 v[8:11], v16
	ds_read_b128 v[12:15], v16 offset:128
	ds_read_b128 v[216:219], v16 offset:8192
	ds_read_b128 v[220:223], v16 offset:8320
	s_waitcnt lgkmcnt(2)
	v_and_b32_e32 v6, 31, v5
	s_waitcnt lgkmcnt(0)
	v_mfma_f32_32x32x16_bf16 v[146:161], v[8:11], v[178:181], v[146:161]
	v_mfma_f32_32x32x16_bf16 v[162:177], v[216:219], v[178:181], v[162:177]
	ds_read_b128 v[8:11], v17
	ds_read_b128 v[216:219], v17 offset:8192
	s_mov_b32 m0, s99
	s_add_u32 s100, s72, 0x0
	s_addc_u32 s101, s73, 0
	global_load_lds_dwordx4 v250, s[100:101]
	s_waitcnt lgkmcnt(2)
	v_mfma_f32_32x32x16_bf16 v[146:161], v[12:15], v[194:197], v[146:161]
	v_mfma_f32_32x32x16_bf16 v[162:177], v[220:223], v[194:197], v[162:177]
	ds_read_b128 v[12:15], v17 offset:128
	ds_read_b128 v[220:223], v17 offset:8320
	s_add_i32 m0, s99, 0x4000
	s_add_u32 s100, s72, 0x100
	s_addc_u32 s101, s73, 0
	global_load_lds_dwordx4 v250, s[100:101]
	s_waitcnt lgkmcnt(2)
	s_waitcnt lgkmcnt(0)
	v_mfma_f32_32x32x16_bf16 v[146:161], v[8:11], v[182:185], v[146:161]
	v_mfma_f32_32x32x16_bf16 v[162:177], v[216:219], v[182:185], v[162:177]
	ds_read_b128 v[8:11], v224
	ds_read_b128 v[216:219], v224 offset:8192
	s_add_i32 m0, s99, 0x2000
	s_add_u32 s100, s72, 0x60000
	s_addc_u32 s101, s73, 0
	global_load_lds_dwordx4 v250, s[100:101]
	s_waitcnt lgkmcnt(2)
	v_mfma_f32_32x32x16_bf16 v[146:161], v[12:15], v[198:201], v[146:161]
	v_mfma_f32_32x32x16_bf16 v[162:177], v[220:223], v[198:201], v[162:177]
	ds_read_b128 v[12:15], v224 offset:128
	ds_read_b128 v[220:223], v224 offset:8320
	s_add_i32 m0, s99, 0x6000
	s_add_u32 s100, s72, 0x60100
	s_addc_u32 s101, s73, 0
	global_load_lds_dwordx4 v250, s[100:101]
	s_waitcnt lgkmcnt(2)
	s_waitcnt lgkmcnt(0)
	v_mfma_f32_32x32x16_bf16 v[146:161], v[8:11], v[186:189], v[146:161]
	v_mfma_f32_32x32x16_bf16 v[162:177], v[216:219], v[186:189], v[162:177]
	ds_read_b128 v[8:11], v2
	ds_read_b128 v[216:219], v2 offset:8192
	s_add_i32 m0, s99, 0x8000
	s_add_u32 s100, s72, 0x1000
	s_addc_u32 s101, s73, 0
	global_load_lds_dwordx4 v251, s[100:101]
	s_waitcnt lgkmcnt(2)
	v_mfma_f32_32x32x16_bf16 v[146:161], v[12:15], v[202:205], v[146:161]
	v_mfma_f32_32x32x16_bf16 v[162:177], v[220:223], v[202:205], v[162:177]
	ds_read_b128 v[12:15], v2 offset:128
	ds_read_b128 v[220:223], v2 offset:8320
	s_add_i32 m0, s99, 0xc000
	s_add_u32 s100, s72, 0x1100
	s_addc_u32 s101, s73, 0
	global_load_lds_dwordx4 v251, s[100:101]
	s_waitcnt lgkmcnt(2)
	s_waitcnt lgkmcnt(0)
	v_mfma_f32_32x32x16_bf16 v[146:161], v[8:11], v[190:193], v[146:161]
	v_mfma_f32_32x32x16_bf16 v[162:177], v[216:219], v[190:193], v[162:177]
	s_add_i32 m0, s99, 0xa000
	s_add_u32 s100, s72, 0x61000
	s_addc_u32 s101, s73, 0
	global_load_lds_dwordx4 v251, s[100:101]
	s_waitcnt lgkmcnt(0)
	v_mfma_f32_32x32x16_bf16 v[146:161], v[12:15], v[206:209], v[146:161]
	v_mfma_f32_32x32x16_bf16 v[162:177], v[220:223], v[206:209], v[162:177]
	s_add_i32 m0, s99, 0xe000
	s_add_u32 s100, s72, 0x61100
	s_addc_u32 s101, s73, 0
	global_load_lds_dwordx4 v251, s[100:101]
	s_cmp_le_i32 s80, s69
	s_cbranch_scc1 .LBB0_1141
; __device__ __forceinline__ void attn_unit_da(const bf16_t* QKV, bf16_t* O, int b, int h, int qb, float slope2, int dmax, bool freeze_ok, const float* const* in, float lambda_init, LAS char* lds) {
;     ...
;                 if (need_mask) { const int kq = k0 - (r0 + r32_t) + 4 * hi_t;
; #pragma unroll
;                     for (int r = 0; r < 16; ++r) { const int kr = kq + (r & 3) + 8 * (r >> 2); if (kr > 0) p0[r] = -INFINITY; if (kr + 32 > 0) p1[r] = -INFINITY; } }
	v_sub_u32_e32 v2, v4, v6
	v_add_u32_e32 v2, s97, v2
	s_movk_i32 s34, 0xffe6
	s_movk_i32 s64, 0xffe5
	s_movk_i32 s30, 0xffe7
	v_cmp_lt_i32_e64 s[62:63], s34, v2
	v_cmp_lt_i32_e64 s[64:65], s64, v2
	s_movk_i32 s28, 0xffe8
	v_cmp_lt_i32_e64 s[60:61], s30, v2
	s_and_b64 s[62:63], s[64:65], s[62:63]
	s_movk_i32 s26, 0xffed
	v_cmp_lt_i32_e64 s[58:59], s28, v2
	s_and_b64 s[60:61], s[62:63], s[60:61]
	s_movk_i32 s24, 0xffee
	v_cmp_lt_i32_e64 s[56:57], s26, v2
	s_and_b64 s[58:59], s[60:61], s[58:59]
	s_movk_i32 s22, 0xffef
	v_cmp_lt_i32_e64 s[54:55], s24, v2
	s_and_b64 s[56:57], s[58:59], s[56:57]
	v_cmp_lt_i32_e64 s[52:53], s22, v2
	s_and_b64 s[54:55], s[56:57], s[54:55]
	v_cmp_lt_i32_e64 s[50:51], -16, v2
	s_and_b64 s[52:53], s[54:55], s[52:53]
	v_cmp_lt_i32_e64 s[48:49], -11, v2
	s_and_b64 s[50:51], s[52:53], s[50:51]
	v_cmp_lt_i32_e64 s[46:47], -10, v2
	s_and_b64 s[48:49], s[50:51], s[48:49]
	v_cmp_lt_i32_e64 s[44:45], -9, v2
	s_and_b64 s[46:47], s[48:49], s[46:47]
	s_movk_i32 s8, 0xffe0
	v_cmp_lt_i32_e64 s[42:43], -8, v2
	s_and_b64 s[44:45], s[46:47], s[44:45]
	v_cmp_gt_i32_e64 s[6:7], 1, v2
	v_cmp_lt_i32_e32 vcc, s8, v2
	v_cmp_gt_i32_e64 s[8:9], 0, v2
	v_cmp_lt_i32_e64 s[40:41], -3, v2
	s_and_b64 s[42:43], s[44:45], s[42:43]
	s_or_b64 s[6:7], s[8:9], s[6:7]
	v_cmp_lt_i32_e64 s[36:37], -2, v2
	s_and_b64 s[40:41], s[42:43], s[40:41]
	v_cndmask_b32_e64 v7, v240, v147, s[8:9]
	v_cndmask_b32_e64 v8, v240, v146, s[6:7]
	s_and_b64 s[36:37], s[40:41], s[36:37]
	s_movk_i32 s34, 0xffc6
	v_cndmask_b32_e64 v146, v146, v8, s[36:37]
	v_cndmask_b32_e64 v148, v148, v240, s[36:37]
	v_cndmask_b32_e64 v147, v147, v7, s[36:37]
	s_movk_i32 s36, 0xffc5
	s_movk_i32 s30, 0xffc7
	v_cmp_lt_i32_e64 s[34:35], s34, v2
	v_cmp_lt_i32_e64 s[36:37], s36, v2
	s_movk_i32 s28, 0xffc8
	v_cmp_lt_i32_e64 s[30:31], s30, v2
	s_and_b64 s[34:35], s[36:37], s[34:35]
	s_movk_i32 s26, 0xffcd
	v_cmp_lt_i32_e64 s[28:29], s28, v2
	s_and_b64 s[30:31], s[34:35], s[30:31]
	s_movk_i32 s24, 0xffce
	v_cmp_lt_i32_e64 s[26:27], s26, v2
	s_and_b64 s[28:29], s[30:31], s[28:29]
	s_movk_i32 s22, 0xffcf
	v_cmp_lt_i32_e64 s[24:25], s24, v2
	s_and_b64 s[26:27], s[28:29], s[26:27]
	s_movk_i32 s20, 0xffd0
	v_cmp_lt_i32_e64 s[22:23], s22, v2
	s_and_b64 s[24:25], s[26:27], s[24:25]
	s_movk_i32 s18, 0xffd5
	v_cmp_lt_i32_e64 s[20:21], s20, v2
	s_and_b64 s[22:23], s[24:25], s[22:23]
	s_movk_i32 s16, 0xffd6
	v_cmp_lt_i32_e64 s[18:19], s18, v2
	s_and_b64 s[20:21], s[22:23], s[20:21]
	s_movk_i32 s14, 0xffd7
	v_cmp_lt_i32_e64 s[16:17], s16, v2
	s_and_b64 s[18:19], s[20:21], s[18:19]
	s_movk_i32 s12, 0xffd8
	v_cmp_lt_i32_e64 s[14:15], s14, v2
	s_and_b64 s[16:17], s[18:19], s[16:17]
	s_movk_i32 s10, 0xffdd
	v_cmp_lt_i32_e64 s[12:13], s12, v2
	s_and_b64 s[14:15], s[16:17], s[14:15]
	s_movk_i32 s8, 0xffde
	v_cmp_lt_i32_e64 s[10:11], s10, v2
	s_and_b64 s[12:13], s[14:15], s[12:13]
	s_movk_i32 s6, 0xffdf
	v_cmp_lt_i32_e64 s[8:9], s8, v2
	s_and_b64 s[10:11], s[12:13], s[10:11]
	v_cmp_lt_i32_e64 s[6:7], s6, v2
	s_and_b64 s[8:9], s[10:11], s[8:9]
	s_and_b64 s[6:7], s[8:9], s[6:7]
	v_cndmask_b32_e64 v154, v154, v240, s[50:51]
	s_mov_b32 s50, 0x42000000
	v_cndmask_b32_e64 v153, v153, v240, s[48:49]
	s_mov_b32 s48, 0x42080000
	v_cndmask_b32_e64 v152, v152, v240, s[46:47]
	s_mov_b32 s46, 0x42200000
	v_cndmask_b32_e64 v150, v150, v240, s[42:43]
	s_mov_b32 s42, 0x42280000
	v_cndmask_b32_e64 v149, v149, v240, s[40:41]
	s_mov_b32 s40, 0x42400000
	v_cndmask_b32_e64 v177, v177, v240, s[36:37]
	s_mov_b32 s36, 0x42480000
	v_cndmask_b32_e64 v176, v176, v240, s[34:35]
	s_mov_b32 s34, 0x42600000
	v_cndmask_b32_e64 v175, v175, v240, s[30:31]
	s_mov_b32 s30, 0x42680000
	v_cndmask_b32_e64 v174, v174, v240, s[28:29]
	s_mov_b32 s28, 0x41d00000
	v_cndmask_b32_e64 v173, v173, v240, s[26:27]
	s_mov_b32 s26, 0x41c00000
	v_cndmask_b32_e64 v172, v172, v240, s[24:25]
	s_mov_b32 s24, 0x41900000
	v_cndmask_b32_e64 v171, v171, v240, s[22:23]
	s_mov_b32 s22, 0x41800000
	v_cndmask_b32_e64 v170, v170, v240, s[20:21]
	s_mov_b32 s20, 0x41200000
	v_cndmask_b32_e64 v169, v169, v240, s[18:19]
	s_mov_b32 s18, 0x41000000
	v_cndmask_b32_e64 v168, v168, v240, s[16:17]
	s_mov_b32 s16, 2.0
	s_and_b64 vcc, s[6:7], vcc
	v_cndmask_b32_e64 v161, v161, v240, s[64:65]
	v_cndmask_b32_e64 v160, v160, v240, s[62:63]
	v_cndmask_b32_e64 v159, v159, v240, s[60:61]
	v_cndmask_b32_e64 v158, v158, v240, s[58:59]
	v_cndmask_b32_e64 v157, v157, v240, s[56:57]
	v_cndmask_b32_e64 v156, v156, v240, s[54:55]
	v_cndmask_b32_e64 v155, v155, v240, s[52:53]
	s_mov_b32 s51, 0x42040000
	s_mov_b32 s49, 0x420c0000
	s_mov_b32 s47, 0x42240000
	v_cndmask_b32_e64 v151, v151, v240, s[44:45]
	s_movk_i32 s45, 0x70
	s_mov_b32 s43, 0x422c0000
	s_mov_b32 s41, 0x42440000
	s_mov_b32 s37, 0x424c0000
	s_mov_b32 s35, 0x42640000
	s_mov_b32 s31, 0x426c0000
	s_mov_b32 s29, 0x41d80000
	s_mov_b32 s27, 0x41c80000
	s_mov_b32 s25, 0x41980000
	s_mov_b32 s23, 0x41880000
	s_mov_b32 s21, 0x41300000
	s_mov_b32 s19, 0x41100000
	s_mov_b32 s17, 0x40400000
	v_cndmask_b32_e64 v167, v167, v240, s[14:15]
	v_cndmask_b32_e64 v166, v166, v240, s[12:13]
	v_cndmask_b32_e64 v165, v165, v240, s[10:11]
	v_cndmask_b32_e64 v164, v164, v240, s[8:9]
	v_cndmask_b32_e64 v163, v163, v240, s[6:7]
	v_cndmask_b32_e32 v162, v162, v240, vcc

; __device__ __forceinline__ void attn_unit_da(const bf16_t* QKV, bf16_t* O, int b, int h, int qb, float slope2, int dmax, bool freeze_ok, const float* const* in, float lambda_init, LAS char* lds) {
;     ...
;     const int NT = 2 * (qb + 1);
;     int kt_lo = 0; { const int lim = q0 - 63 - dmax; kt_lo = lim > 0 ? (lim + 63) / 64 : 0; }
;     const int NIT = NT - kt_lo;
;     DMA_DA((NT - 1) * KVBLK, 0);
;     float m_run = -1e30f, l_run = 0.f;
;     for (int it = 0; it < NIT; ++it) {
;         const int k0 = (NT - 1 - it) * KVBLK, bf = it & 1;
;         asm volatile("s_waitcnt vmcnt(0)" ::: "memory");
;         __syncthreads();
;         if (it + 1 < NIT) DMA_DA((NT - 2 - it) * KVBLK, bf ^ 1);
.Lda_inactive:
	s_or_b64 exec, exec, s[76:77]
	v_cmp_lt_i32_e32 vcc, s86, v211
	s_and_saveexec_b64 s[6:7], vcc
	s_cbranch_execz .Lda_inact_done
	v_mov_b32_e32 v8, v230
	s_lshl_b32 s9, s8, 16
	v_ashrrev_i32_e32 v2, 4, v8
	v_lshlrev_b32_e32 v4, 4, v8
	v_and_b32_e32 v4, 0xf0, v4
	v_add_lshl_u32 v5, v2, s71, 4
	v_bitop3_b32 v4, v5, v4, s45 bitop3:0x6c
	v_lshrrev_b32_e32 v9, 1, v4
	v_ashrrev_i32_e32 v4, 5, v8
	v_add_u32_e32 v10, s90, v4
	v_lshrrev_b32_e32 v4, 1, v8
	v_and_b32_e32 v6, 8, v4
	v_lshlrev_b32_e32 v4, 3, v8
	s_xor_b32 s9, s9, 0x10000
	v_mul_lo_u32 v15, v2, s79
	v_and_b32_e32 v12, 24, v4
	v_lshlrev_b32_e32 v4, 5, v10
	s_add_i32 s9, s91, s9
	v_add3_u32 v2, s81, v9, v15
	v_and_b32_e32 v14, 0x60, v4
	s_add_i32 s10, s9, 0x4000
	v_lshl_add_u64 v[4:5], v[2:3], 1, s[72:73]
	s_mov_b32 m0, s9
	v_lshlrev_b32_e32 v7, 1, v10
	global_load_lds_dwordx4 v[4:5], off
	s_mov_b32 m0, s10
	s_mov_b32 s10, 0x1ffff0
	v_bfe_u32 v11, v8, 2, 2
	v_and_b32_e32 v13, 4, v10
	v_and_or_b32 v2, v7, s10, v6
	v_or3_b32 v2, v2, v13, v11
	v_mul_u32_u24_e32 v2, 0x1800, v2
	v_lshl_add_u64 v[4:5], v[4:5], 0, s[38:39]
	v_or3_b32 v2, v2, v14, v12
	s_add_i32 s11, s9, 0x8000
	global_load_lds_dwordx4 v[4:5], off
	v_lshl_add_u64 v[4:5], v[2:3], 1, s[72:73]
	s_add_i32 s12, s9, 0xc000
	v_lshl_add_u64 v[6:7], v[4:5], 0, s[88:89]
	s_mov_b32 m0, s11
	v_lshl_add_u64 v[4:5], v[4:5], 0, s[84:85]
	global_load_lds_dwordx4 v[6:7], off
	s_mov_b32 m0, s12
	v_add3_u32 v2, s87, v9, v15
	global_load_lds_dwordx4 v[4:5], off
	v_lshl_add_u64 v[4:5], v[2:3], 1, s[72:73]
	s_add_i32 m0, s9, 0x2000
	v_lshrrev_b32_e32 v2, 3, v10
	global_load_lds_dwordx4 v[4:5], off
	v_lshl_add_u64 v[4:5], v[4:5], 0, s[38:39]
	s_add_i32 m0, s9, 0x6000
	s_mov_b32 s10, 0x18000
	global_load_lds_dwordx4 v[4:5], off
	v_mul_lo_u32 v2, v2, s10
	v_bfe_u32 v4, v8, 4, 1
	s_mov_b32 s10, 0xc000
	v_mad_u32_u24 v2, v4, s10, v2
	v_bfe_u32 v4, v10, 2, 1
	v_mul_u32_u24_e32 v4, 0x6000, v4
	v_mul_u32_u24_e32 v5, 0x1800, v11
	v_add3_u32 v2, v2, v4, v5
	v_or3_b32 v2, v2, v14, v12
	v_add_u32_e32 v2, 0x30000, v2
	v_lshl_add_u64 v[4:5], v[2:3], 1, s[72:73]
	v_lshl_add_u64 v[6:7], v[4:5], 0, s[88:89]
	s_add_i32 m0, s9, 0xa000
	v_lshl_add_u64 v[4:5], v[4:5], 0, s[84:85]
	global_load_lds_dwordx4 v[6:7], off
	s_add_i32 m0, s9, 0xe000
	s_nop 0
	global_load_lds_dwordx4 v[4:5], off
.Lda_inact_done:
	s_or_b64 exec, exec, s[6:7]
	s_branch .LBB0_1135

; #define LAS __attribute__((address_space(3)))
; #define SEAM(k) do { if (IN((k) + 1)) { xcd_barrier(bar); xcd_barrier(bar); } } while (0)
; #define SEAM(k) do { if (IN((k) + 1)) xcd_barrier(bar); } while (0)
; __global__ void __launch_bounds__(NTHREADS, 2) mega_fwd(Args args) {
;     extern __shared__ __attribute__((aligned(16))) unsigned char lds_raw[];
;     Frame F; F.lds = (LAS unsigned char*)lds_raw; F.tid = threadIdx.x; F.lane = F.tid & 63; F.wave = __builtin_amdgcn_readfirstlane(F.tid >> 6);
;     F.bid = blockIdx.x; F.G = gridDim.x; F.gw = F.bid * NWAVES + F.wave; F.NGW = F.G * NWAVES;
;     volatile LAS unsigned* MISC = (volatile LAS unsigned*)(F.lds + MISC_OFF);
;     if (F.tid < 32) MISC[F.tid] = 0u;
;     if (F.tid == 0) *(volatile LAS int*)(F.lds + TAB_MISC + 512) = 0;
;     __syncthreads();
;     unsigned char* ws = args.ws;
;     unsigned* ctl = (unsigned*)(ws + WS_CTL);
;     const int lo = args.ph_lo, hi = args.ph_hi;
;     const bool multi = (hi - lo) > 1;
;     unsigned* barw = ctl + CW_BAR + args.li * XCD_BAR_WORDS;
;     XcdBarrier bar; bar.bar = barw; bar.x = 0; bar.st = nullptr;
;     if (multi) bar = xcd_barrier_post(barw, MISC + 8);
;     if (IN(0)) { p0_prologue(F, args); SEAM(0); }
;     WorkerState W; W.nC = (int)gridDim.x - NWORK; W.isw = (int)blockIdx.x >= W.nC; W.stride = NWORK * NWAVES;
;     { const int ww = ((int)blockIdx.x - W.nC) * NWAVES + F.wave, base = need_before(lo > 1 ? lo : 1); W.nxt = base + (((ww - base) % W.stride) + W.stride) % W.stride; }
;     F.G = W.nC; F.NGW = W.nC * NWAVES;
;     layer_body<0>(F, args, bar, lo, hi, W);
;     W.isw = false; W.nC = (int)gridDim.x; F.G = (int)gridDim.x; F.NGW = F.G * NWAVES;
;     layer_body<1>(F, args, bar, lo, hi, W);
; }
	.amdhsa_kernel _Z8mega_fwd4Args
		.amdhsa_group_segment_fixed_size 0
		.amdhsa_private_segment_fixed_size 0
		.amdhsa_kernarg_size 472
		.amdhsa_user_sgpr_count 2
		.amdhsa_user_sgpr_dispatch_ptr 0
		.amdhsa_user_sgpr_queue_ptr 0
		.amdhsa_user_sgpr_kernarg_segment_ptr 1
		.amdhsa_user_sgpr_dispatch_id 0
		.amdhsa_user_sgpr_kernarg_preload_length 0
		.amdhsa_user_sgpr_kernarg_preload_offset 0
		.amdhsa_user_sgpr_private_segment_size 0
		.amdhsa_uses_dynamic_stack 0
		.amdhsa_enable_private_segment 0
		.amdhsa_system_sgpr_workgroup_id_x 1
		.amdhsa_system_sgpr_workgroup_id_y 0
		.amdhsa_system_sgpr_workgroup_id_z 0
		.amdhsa_system_sgpr_workgroup_info 0
		.amdhsa_system_vgpr_workitem_id 0
		.amdhsa_next_free_vgpr 256
		.amdhsa_next_free_sgpr 102
		.amdhsa_accum_offset 256
		.amdhsa_reserve_vcc 1
		.amdhsa_float_round_mode_32 0
		.amdhsa_float_round_mode_16_64 0
		.amdhsa_float_denorm_mode_32 3
		.amdhsa_float_denorm_mode_16_64 3
		.amdhsa_dx10_clamp 1
		.amdhsa_ieee_mode 1
		.amdhsa_fp16_overflow 0
		.amdhsa_tg_split 0
		.amdhsa_exception_fp_ieee_invalid_op 0
		.amdhsa_exception_fp_denorm_src 0
		.amdhsa_exception_fp_ieee_div_zero 0
		.amdhsa_exception_fp_ieee_overflow 0
		.amdhsa_exception_fp_ieee_underflow 0
		.amdhsa_exception_fp_ieee_inexact 0
		.amdhsa_exception_int_div_zero 0
	.end_amdhsa_kernel

; #define LAS __attribute__((address_space(3)))
; #define SEAM(k) do { if (IN((k) + 1)) { xcd_barrier(bar); xcd_barrier(bar); } } while (0)
; #define SEAM(k) do { if (IN((k) + 1)) xcd_barrier(bar); } while (0)
; __global__ void __launch_bounds__(NTHREADS, 2) mega_fwd(Args args) {
;     extern __shared__ __attribute__((aligned(16))) unsigned char lds_raw[];
;     Frame F; F.lds = (LAS unsigned char*)lds_raw; F.tid = threadIdx.x; F.lane = F.tid & 63; F.wave = __builtin_amdgcn_readfirstlane(F.tid >> 6);
;     F.bid = blockIdx.x; F.G = gridDim.x; F.gw = F.bid * NWAVES + F.wave; F.NGW = F.G * NWAVES;
;     volatile LAS unsigned* MISC = (volatile LAS unsigned*)(F.lds + MISC_OFF);
;     if (F.tid < 32) MISC[F.tid] = 0u;
;     if (F.tid == 0) *(volatile LAS int*)(F.lds + TAB_MISC + 512) = 0;
;     __syncthreads();
;     unsigned char* ws = args.ws;
;     unsigned* ctl = (unsigned*)(ws + WS_CTL);
;     const int lo = args.ph_lo, hi = args.ph_hi;
;     const bool multi = (hi - lo) > 1;
;     unsigned* barw = ctl + CW_BAR + args.li * XCD_BAR_WORDS;
;     XcdBarrier bar; bar.bar = barw; bar.x = 0; bar.st = nullptr;
;     if (multi) bar = xcd_barrier_post(barw, MISC + 8);
;     if (IN(0)) { p0_prologue(F, args); SEAM(0); }
;     WorkerState W; W.nC = (int)gridDim.x - NWORK; W.isw = (int)blockIdx.x >= W.nC; W.stride = NWORK * NWAVES;
;     { const int ww = ((int)blockIdx.x - W.nC) * NWAVES + F.wave, base = need_before(lo > 1 ? lo : 1); W.nxt = base + (((ww - base) % W.stride) + W.stride) % W.stride; }
;     F.G = W.nC; F.NGW = W.nC * NWAVES;
;     layer_body<0>(F, args, bar, lo, hi, W);
;     W.isw = false; W.nC = (int)gridDim.x; F.G = (int)gridDim.x; F.NGW = F.G * NWAVES;
;     layer_body<1>(F, args, bar, lo, hi, W);
; }
amdhsa.kernels:
  - .agpr_count:     0
    .args:
      - .offset:         0
        .size:           216
        .value_kind:     by_value
      - .offset:         216
        .size:           4
        .value_kind:     hidden_block_count_x
      - .offset:         220
        .size:           4
        .value_kind:     hidden_block_count_y
      - .offset:         224
        .size:           4
        .value_kind:     hidden_block_count_z
      - .offset:         228
        .size:           2
        .value_kind:     hidden_group_size_x
      - .offset:         230
        .size:           2
        .value_kind:     hidden_group_size_y
      - .offset:         232
        .size:           2
        .value_kind:     hidden_group_size_z
      - .offset:         234
        .size:           2
        .value_kind:     hidden_remainder_x
      - .offset:         236
        .size:           2
        .value_kind:     hidden_remainder_y
      - .offset:         238
        .size:           2
        .value_kind:     hidden_remainder_z
      - .offset:         256
        .size:           8
        .value_kind:     hidden_global_offset_x
      - .offset:         264
        .size:           8
        .value_kind:     hidden_global_offset_y
      - .offset:         272
        .size:           8
        .value_kind:     hidden_global_offset_z
      - .offset:         280
        .size:           2
        .value_kind:     hidden_grid_dims
      - .offset:         336
        .size:           4
        .value_kind:     hidden_dynamic_lds_size
    .group_segment_fixed_size: 0
    .kernarg_segment_align: 8
    .kernarg_segment_size: 472
    .language:       OpenCL C
    .language_version:
      - 2
      - 0
    .max_flat_workgroup_size: 512
    .name:           _Z8mega_fwd4Args
    .private_segment_fixed_size: 0
    .sgpr_count:     108
    .sgpr_spill_count: 50
    .symbol:         _Z8mega_fwd4Args.kd
    .uniform_work_group_size: 1
    .uses_dynamic_stack: false
    .vgpr_count:     256
    .vgpr_spill_count: 0
    .wavefront_size: 64
